# router list append: the two returning position atomics of a token pair issued together with counted waits (were atomic + vmcnt(0) twice in series)
# speedup vs baseline: 1.0047x; 1.0038x over previous
.LBB0_1220:
	v_cmp_gt_f32_e64 s[0:1], v27, v20
	v_cmp_eq_u32_e32 vcc, v152, v22
	v_add_u32_e32 v22, 1, v22
	v_cndmask_b32_e64 v23, v20, v27, s[0:1]
	v_cndmask_b32_e64 v24, v152, v156, s[0:1]
	v_cmp_gt_f32_e64 s[0:1], v25, v23
	s_nop 1
	v_cndmask_b32_e64 v23, v23, v25, s[0:1]
	v_cndmask_b32_e64 v24, v24, v157, s[0:1]
	v_cmp_gt_f32_e64 s[0:1], v15, v23
	s_nop 1
	v_cndmask_b32_e64 v23, v23, v15, s[0:1]
	v_max_f32_e32 v28, v23, v23
	v_cndmask_b32_e64 v24, v24, v158, s[0:1]
	v_mov_b32_dpp v26, v23 quad_perm:[1,0,3,2] row_mask:0xf bank_mask:0xf bound_ctrl:1
	v_max_f32_e32 v26, v26, v26
	v_max_f32_e32 v26, v28, v26
	s_nop 1
	v_mov_b32_dpp v28, v26 quad_perm:[2,3,0,1] row_mask:0xf bank_mask:0xf bound_ctrl:1
	v_max_f32_e32 v28, v28, v28
	v_max_f32_e32 v26, v26, v28
	s_nop 1
	v_mov_b32_dpp v28, v26 row_half_mirror row_mask:0xf bank_mask:0xf bound_ctrl:1
	v_max_f32_e32 v28, v28, v28
	v_max_f32_e32 v26, v26, v28
	s_nop 1
	v_mov_b32_dpp v28, v26 row_mirror row_mask:0xf bank_mask:0xf bound_ctrl:1
	v_max_f32_e32 v28, v28, v28
	v_max_f32_e32 v26, v26, v28
	s_nop 0
	v_readlane_b32 s8, v26, 32
	v_readlane_b32 s9, v26, 48
	v_readlane_b32 s0, v26, 0
	v_readlane_b32 s1, v26, 16
	v_max_f32_e64 v26, s9, s9
	v_max_f32_e64 v28, s8, s8
	v_max_f32_e32 v26, v28, v26
	v_mov_b32_e32 v28, s1
	v_max3_f32 v26, s0, v28, v26
	v_cmp_eq_f32_e64 s[0:1], v23, v26
	s_nop 1
	v_cndmask_b32_e64 v23, v230, v24, s[0:1]
	s_nop 1
	v_min_i32_dpp v23, v23, v23 quad_perm:[1,0,3,2] row_mask:0xf bank_mask:0xf bound_ctrl:1
	s_nop 1
	v_min_i32_dpp v23, v23, v23 quad_perm:[2,3,0,1] row_mask:0xf bank_mask:0xf bound_ctrl:1
	s_nop 1
	v_min_i32_dpp v23, v23, v23 row_half_mirror row_mask:0xf bank_mask:0xf bound_ctrl:1
	s_nop 1
	v_min_i32_dpp v23, v23, v23 row_mirror row_mask:0xf bank_mask:0xf bound_ctrl:1
	s_nop 0
	v_readlane_b32 s8, v23, 32
	v_readlane_b32 s9, v23, 48
	v_readlane_b32 s1, v23, 16
	s_min_i32 s8, s8, s9
	v_readlane_b32 s0, v23, 0
	v_mov_b32_e32 v23, s1
	v_mov_b32_e32 v24, s8
	v_min3_i32 v23, s0, v23, v24
	v_and_b32_e32 v24, 63, v23
	v_readfirstlane_b32 s8, v23
	s_ashr_i32 s9, s8, 6
	s_cmp_eq_u32 s9, 1
	s_cselect_b64 s[46:47], -1, 0
	s_cmp_eq_u32 s9, 2
	v_cmp_gt_u32_e64 s[0:1], 64, v23
	s_cselect_b64 s[50:51], -1, 0
	s_cmp_eq_u32 s9, 3
	v_cmp_eq_u32_e64 s[54:55], v152, v24
	v_cndmask_b32_e64 v26, 0, v7, s[0:1]
	v_cndmask_b32_e64 v28, 0, v8, s[46:47]
	s_cselect_b64 s[52:53], -1, 0
	s_and_b64 s[0:1], s[0:1], s[54:55]
	v_add_f32_e32 v26, v26, v28
	v_cndmask_b32_e64 v28, 0, v9, s[50:51]
	v_cndmask_b32_e64 v29, 0, v10, s[52:53]
	v_cndmask_b32_e64 v20, v20, v228, s[0:1]
	s_and_b64 s[0:1], s[54:55], s[46:47]
	v_add_f32_e32 v28, v28, v29
	v_cndmask_b32_e64 v27, v27, v228, s[0:1]
	s_and_b64 s[0:1], s[54:55], s[50:51]
	v_add_f32_e32 v26, v26, v28
	v_cndmask_b32_e64 v25, v25, v228, s[0:1]
	s_and_b64 s[0:1], s[54:55], s[52:53]
	v_cndmask_b32_e64 v15, v15, v228, s[0:1]
	v_readlane_b32 s65, v26, s8
	v_cmp_gt_f32_e64 s[0:1], v17, v16
	v_cndmask_b32_e32 v6, v6, v23, vcc
	v_mov_b32_e32 v24, s65
	v_cndmask_b32_e64 v23, v16, v17, s[0:1]
	v_cndmask_b32_e32 v18, v18, v24, vcc
	v_cndmask_b32_e64 v24, v152, v156, s[0:1]
	v_cmp_gt_f32_e64 s[0:1], v19, v23
	s_nop 1
	v_cndmask_b32_e64 v23, v23, v19, s[0:1]
	v_cndmask_b32_e64 v24, v24, v157, s[0:1]
	v_cmp_gt_f32_e64 s[0:1], v21, v23
	s_nop 1
	v_cndmask_b32_e64 v23, v23, v21, s[0:1]
	v_max_f32_e32 v28, v23, v23
	v_cndmask_b32_e64 v24, v24, v158, s[0:1]
	v_mov_b32_dpp v26, v23 quad_perm:[1,0,3,2] row_mask:0xf bank_mask:0xf bound_ctrl:1
	v_max_f32_e32 v26, v26, v26
	v_max_f32_e32 v26, v28, v26
	s_nop 1
	v_mov_b32_dpp v28, v26 quad_perm:[2,3,0,1] row_mask:0xf bank_mask:0xf bound_ctrl:1
	v_max_f32_e32 v28, v28, v28
	v_max_f32_e32 v26, v26, v28
	s_nop 1
	v_mov_b32_dpp v28, v26 row_half_mirror row_mask:0xf bank_mask:0xf bound_ctrl:1
	v_max_f32_e32 v28, v28, v28
	v_max_f32_e32 v26, v26, v28
	s_nop 1
	v_mov_b32_dpp v28, v26 row_mirror row_mask:0xf bank_mask:0xf bound_ctrl:1
	v_max_f32_e32 v28, v28, v28
	v_max_f32_e32 v26, v26, v28
	s_nop 0
	v_readlane_b32 s8, v26, 32
	v_readlane_b32 s9, v26, 48
	v_readlane_b32 s0, v26, 0
	v_readlane_b32 s1, v26, 16
	v_max_f32_e64 v26, s9, s9
	v_max_f32_e64 v28, s8, s8
	v_max_f32_e32 v26, v28, v26
	v_mov_b32_e32 v28, s1
	v_max3_f32 v26, s0, v28, v26
	v_cmp_eq_f32_e64 s[0:1], v23, v26
	s_nop 1
	v_cndmask_b32_e64 v23, v230, v24, s[0:1]
	s_nop 1
	v_min_i32_dpp v23, v23, v23 quad_perm:[1,0,3,2] row_mask:0xf bank_mask:0xf bound_ctrl:1
	s_nop 1
	v_min_i32_dpp v23, v23, v23 quad_perm:[2,3,0,1] row_mask:0xf bank_mask:0xf bound_ctrl:1
	s_nop 1
	v_min_i32_dpp v23, v23, v23 row_half_mirror row_mask:0xf bank_mask:0xf bound_ctrl:1
	s_nop 1
	v_min_i32_dpp v23, v23, v23 row_mirror row_mask:0xf bank_mask:0xf bound_ctrl:1
	s_nop 0
	v_readlane_b32 s8, v23, 32
	v_readlane_b32 s9, v23, 48
	v_readlane_b32 s1, v23, 16
	s_min_i32 s8, s8, s9
	v_readlane_b32 s0, v23, 0
	v_mov_b32_e32 v23, s1
	v_mov_b32_e32 v24, s8
	v_min3_i32 v23, s0, v23, v24
	v_cmp_gt_u32_e64 s[0:1], 64, v23
	v_readfirstlane_b32 s8, v23
	s_ashr_i32 s9, s8, 6
	s_cmp_eq_u32 s9, 1
	s_cselect_b64 s[46:47], -1, 0
	s_cmp_eq_u32 s9, 2
	s_cselect_b64 s[50:51], -1, 0
	s_cmp_eq_u32 s9, 3
	v_cndmask_b32_e64 v26, 0, v11, s[0:1]
	v_cndmask_b32_e64 v28, 0, v12, s[46:47]
	s_cselect_b64 s[52:53], -1, 0
	v_and_b32_e32 v24, 63, v23
	v_add_f32_e32 v26, v26, v28
	v_cndmask_b32_e64 v28, 0, v13, s[50:51]
	v_cndmask_b32_e64 v29, 0, v14, s[52:53]
	v_add_f32_e32 v28, v28, v29
	v_cmp_eq_u32_e64 s[54:55], v152, v24
	v_add_f32_e32 v26, v26, v28
	s_and_b64 s[0:1], s[0:1], s[54:55]
	v_cndmask_b32_e64 v16, v16, v228, s[0:1]
	s_and_b64 s[0:1], s[54:55], s[46:47]
	v_readlane_b32 s64, v26, s8
	v_cndmask_b32_e64 v17, v17, v228, s[0:1]
	s_and_b64 s[0:1], s[54:55], s[50:51]
	v_mov_b32_e32 v24, s64
	v_cndmask_b32_e64 v19, v19, v228, s[0:1]
	s_and_b64 s[0:1], s[54:55], s[52:53]
	v_cndmask_b32_e32 v3, v3, v24, vcc
	v_cndmask_b32_e32 v2, v2, v23, vcc
	v_cmp_eq_u32_e32 vcc, 8, v22
	v_cndmask_b32_e64 v21, v21, v228, s[0:1]
	v_pk_add_f32 v[4:5], v[4:5], s[64:65]
	s_cbranch_vccz .LBB0_1220
	s_and_saveexec_b64 s[0:1], s[44:45]
	s_mov_b32 s94, 0x3fb8aa3b
	s_mov_b32 s95, 0xc2ce8ed0
	s_mov_b32 s96, 0x42b17218
	s_mov_b64 s[92:93], 0x1fffff
	s_cbranch_execz .LBB0_1050
	v_div_scale_f32 v7, s[8:9], v5, v5, v18
	v_rcp_f32_e32 v9, v7
	s_add_i32 s15, s15, s3
	v_lshl_or_b32 v8, s15, 3, v152
	v_fma_f32 v10, -v7, v9, 1.0
	v_fmac_f32_e32 v9, v10, v9
	v_div_scale_f32 v10, vcc, v18, v5, v18
	v_mul_f32_e32 v11, v10, v9
	v_fma_f32 v12, -v7, v11, v10
	v_fmac_f32_e32 v11, v12, v9
	v_fma_f32 v7, -v7, v11, v10
	v_div_fmas_f32 v7, v7, v9, v11
	v_div_fixup_f32 v5, v7, v5, v18
	v_ashrrev_i32_e32 v9, 31, v8
	v_mul_f32_e32 v5, 0x40200000, v5
	v_lshl_add_u64 v[10:11], v[8:9], 2, s[36:37]
	global_store_dword v[10:11], v5, off
	v_lshlrev_b32_e32 v10, 5, v6
	v_ashrrev_i32_e32 v11, 31, v10
	v_lshl_add_u64 v[10:11], v[10:11], 2, s[16:17]
	global_atomic_add v10, v[10:11], v221, off sc0
	v_lshlrev_b32_e32 v12, 5, v2
	v_ashrrev_i32_e32 v13, 31, v12
	v_lshl_add_u64 v[12:13], v[12:13], 2, s[16:17]
	global_atomic_add v12, v[12:13], v221, off sc0
	v_ashrrev_i32_e32 v7, 31, v6
	v_lshlrev_b64 v[6:7], 16, v[6:7]
	v_lshl_add_u64 v[6:7], s[48:49], 0, v[6:7]
	v_div_scale_f32 v5, s[8:9], v4, v4, v3
	s_waitcnt vmcnt(1)
	v_ashrrev_i32_e32 v11, 31, v10
	v_lshl_add_u64 v[6:7], v[10:11], 2, v[6:7]
	global_store_dword v[6:7], v8, off
	v_rcp_f32_e32 v7, v5
	v_or_b32_e32 v6, 8, v8
	v_fma_f32 v8, -v5, v7, 1.0
	v_fmac_f32_e32 v7, v8, v7
	v_div_scale_f32 v8, vcc, v3, v4, v3
	v_mul_f32_e32 v9, v8, v7
	v_fma_f32 v10, -v5, v9, v8
	v_fmac_f32_e32 v9, v10, v7
	v_fma_f32 v5, -v5, v9, v8
	v_div_fmas_f32 v5, v5, v7, v9
	v_div_fixup_f32 v3, v5, v4, v3
	v_ashrrev_i32_e32 v7, 31, v6
	v_mul_f32_e32 v3, 0x40200000, v3
	v_lshl_add_u64 v[4:5], v[6:7], 2, s[36:37]
	global_store_dword v[4:5], v3, off
	v_ashrrev_i32_e32 v3, 31, v2
	v_lshlrev_b64 v[2:3], 16, v[2:3]
	v_lshl_add_u64 v[2:3], s[48:49], 0, v[2:3]
	s_waitcnt vmcnt(2)
	v_ashrrev_i32_e32 v13, 31, v12
	v_lshl_add_u64 v[2:3], v[12:13], 2, v[2:3]
	global_store_dword v[2:3], v6, off
	s_branch .LBB0_1050
